# speedup vs baseline: 1.1264x; 1.0311x over previous
.LBB0_15:
	s_and_b64 vcc, exec, s[8:9]
	s_cbranch_vccz .LBB0_22
	s_waitcnt lgkmcnt(0)
	s_load_dwordx2 s[4:5], s[0:1], 0x50
	s_add_i32 s3, s2, 0xffffea00
	s_movk_i32 s8, 0x240
	s_lshr_b32 s3, s3, 2
	s_and_b32 s16, s2, 3
	v_cmp_gt_u32_e32 vcc, s8, v0
	s_and_saveexec_b64 s[8:9], vcc
	s_cbranch_execz .LBB0_19
	s_load_dwordx2 s[10:11], s[0:1], 0x20
	s_lshl_b32 s12, s3, 8
	s_lshl_b32 s13, s16, 6
	s_or_b32 s12, s12, s13
	s_mul_hi_u32 s13, s12, 36
	s_mul_i32 s12, s12, 36
	v_mov_b32_e32 v3, 0
	s_waitcnt lgkmcnt(0)
	s_add_u32 s10, s10, s12
	v_mov_b32_e32 v1, v3
	s_addc_u32 s11, s11, s13
	s_mov_b64 s[12:13], 0
	s_mov_b32 s17, 0xe38f
	s_mov_b32 s18, 0x42000000
	s_movk_i32 s19, 0x90
	s_mov_b64 s[14:15], 0x100
	s_movk_i32 s20, 0x13f
	v_mov_b64_e32 v[4:5], v[0:1]
	v_lshlrev_b32_e32 v6, 2, v0
	global_load_dword v10, v6, s[10:11] nt
	global_load_dword v11, v6, s[10:11] offset:1024 nt
	v_cmp_gt_u32_e32 vcc, 64, v0
	s_and_saveexec_b64 s[12:13], vcc
	global_load_dword v12, v6, s[10:11] offset:2048 nt
	s_mov_b64 exec, s[12:13]
	s_movk_i32 s14, 0xfaf2
	v_mul_u32_u24_e32 v8, 0xe38f, v0
	v_lshrrev_b32_e32 v8, 19, v8
	v_mul_u32_u24_e32 v9, 0x90, v0
	v_mad_i32_i24 v13, v8, s14, v9
	v_add_u32_e32 v7, 0x100, v0
	v_mul_u32_u24_e32 v8, 0xe38f, v7
	v_lshrrev_b32_e32 v8, 19, v8
	v_mul_u32_u24_e32 v9, 0x90, v7
	v_mad_i32_i24 v14, v8, s14, v9
	v_add_u32_e32 v7, 0x200, v0
	v_mul_u32_u24_e32 v8, 0xe38f, v7
	v_lshrrev_b32_e32 v8, 19, v8
	v_mul_u32_u24_e32 v9, 0x90, v7
	v_mad_i32_i24 v15, v8, s14, v9
	s_waitcnt vmcnt(0)
	v_fma_mixlo_f16 v1, v10, s18, 0
	v_fma_mixlo_f16 v2, v11, s18, 0
	ds_write_b16 v13, v1
	ds_write_b16 v14, v2
	s_and_saveexec_b64 s[12:13], vcc
	v_fma_mixlo_f16 v3, v12, s18, 0
	ds_write_b16 v15, v3
	s_mov_b64 exec, s[12:13]

.LBB0_23:
	s_and_b64 vcc, exec, s[8:9]
	s_cbranch_vccz .LBB0_30
	s_waitcnt lgkmcnt(0)
	s_load_dwordx2 s[4:5], s[0:1], 0x48
	s_add_i32 s3, s2, 0xfffff200
	s_movk_i32 s8, 0x240
	s_lshr_b32 s3, s3, 3
	s_and_b32 s16, s2, 7
	v_cmp_gt_u32_e32 vcc, s8, v0
	s_and_saveexec_b64 s[8:9], vcc
	s_cbranch_execz .LBB0_27
	s_load_dwordx2 s[10:11], s[0:1], 0x18
	s_lshl_b32 s12, s3, 9
	s_lshl_b32 s13, s16, 6
	s_or_b32 s12, s12, s13
	s_mul_hi_u32 s13, s12, 36
	s_mul_i32 s12, s12, 36
	v_mov_b32_e32 v3, 0
	s_waitcnt lgkmcnt(0)
	s_add_u32 s10, s10, s12
	v_mov_b32_e32 v1, v3
	s_addc_u32 s11, s11, s13
	s_mov_b64 s[12:13], 0
	s_mov_b32 s17, 0xe38f
	s_mov_b32 s18, 0x42000000
	s_movk_i32 s19, 0x90
	s_mov_b64 s[14:15], 0x100
	s_movk_i32 s20, 0x13f
	v_mov_b64_e32 v[4:5], v[0:1]
	v_lshlrev_b32_e32 v6, 2, v0
	global_load_dword v10, v6, s[10:11] nt
	global_load_dword v11, v6, s[10:11] offset:1024 nt
	v_cmp_gt_u32_e32 vcc, 64, v0
	s_and_saveexec_b64 s[12:13], vcc
	global_load_dword v12, v6, s[10:11] offset:2048 nt
	s_mov_b64 exec, s[12:13]
	s_movk_i32 s14, 0xfaf2
	v_mul_u32_u24_e32 v8, 0xe38f, v0
	v_lshrrev_b32_e32 v8, 19, v8
	v_mul_u32_u24_e32 v9, 0x90, v0
	v_mad_i32_i24 v13, v8, s14, v9
	v_add_u32_e32 v7, 0x100, v0
	v_mul_u32_u24_e32 v8, 0xe38f, v7
	v_lshrrev_b32_e32 v8, 19, v8
	v_mul_u32_u24_e32 v9, 0x90, v7
	v_mad_i32_i24 v14, v8, s14, v9
	v_add_u32_e32 v7, 0x200, v0
	v_mul_u32_u24_e32 v8, 0xe38f, v7
	v_lshrrev_b32_e32 v8, 19, v8
	v_mul_u32_u24_e32 v9, 0x90, v7
	v_mad_i32_i24 v15, v8, s14, v9
	s_waitcnt vmcnt(0)
	v_fma_mixlo_f16 v1, v10, s18, 0
	v_fma_mixlo_f16 v2, v11, s18, 0
	ds_write_b16 v13, v1
	ds_write_b16 v14, v2
	s_and_saveexec_b64 s[12:13], vcc
	v_fma_mixlo_f16 v3, v12, s18, 0
	ds_write_b16 v15, v3
	s_mov_b64 exec, s[12:13]

.LBB0_31:
	s_waitcnt lgkmcnt(0)
	s_load_dwordx2 s[4:5], s[0:1], 0x40
	s_add_i32 s3, s2, 0xfffffa00
	s_movk_i32 s8, 0x240
	s_lshr_b32 s3, s3, 2
	s_and_b32 s16, s2, 3
	v_cmp_gt_u32_e32 vcc, s8, v0
	s_and_saveexec_b64 s[8:9], vcc
	s_cbranch_execz .LBB0_34
	s_load_dwordx2 s[10:11], s[0:1], 0x10
	s_lshl_b32 s12, s3, 8
	s_lshl_b32 s13, s16, 6
	s_or_b32 s12, s12, s13
	s_mul_hi_u32 s13, s12, 36
	s_mul_i32 s12, s12, 36
	v_mov_b32_e32 v3, 0
	s_waitcnt lgkmcnt(0)
	s_add_u32 s10, s10, s12
	v_mov_b32_e32 v1, v3
	s_addc_u32 s11, s11, s13
	s_mov_b64 s[12:13], 0
	s_mov_b32 s17, 0xe38f
	s_mov_b32 s18, 0x42000000
	s_movk_i32 s19, 0x90
	s_mov_b64 s[14:15], 0x100
	s_movk_i32 s20, 0x13f
	v_mov_b64_e32 v[4:5], v[0:1]
	v_lshlrev_b32_e32 v6, 2, v0
	global_load_dword v10, v6, s[10:11] nt
	global_load_dword v11, v6, s[10:11] offset:1024 nt
	v_cmp_gt_u32_e32 vcc, 64, v0
	s_and_saveexec_b64 s[12:13], vcc
	global_load_dword v12, v6, s[10:11] offset:2048 nt
	s_mov_b64 exec, s[12:13]
	s_movk_i32 s14, 0xfaf2
	v_mul_u32_u24_e32 v8, 0xe38f, v0
	v_lshrrev_b32_e32 v8, 19, v8
	v_mul_u32_u24_e32 v9, 0x90, v0
	v_mad_i32_i24 v13, v8, s14, v9
	v_add_u32_e32 v7, 0x100, v0
	v_mul_u32_u24_e32 v8, 0xe38f, v7
	v_lshrrev_b32_e32 v8, 19, v8
	v_mul_u32_u24_e32 v9, 0x90, v7
	v_mad_i32_i24 v14, v8, s14, v9
	v_add_u32_e32 v7, 0x200, v0
	v_mul_u32_u24_e32 v8, 0xe38f, v7
	v_lshrrev_b32_e32 v8, 19, v8
	v_mul_u32_u24_e32 v9, 0x90, v7
	v_mad_i32_i24 v15, v8, s14, v9
	s_waitcnt vmcnt(0)
	v_fma_mixlo_f16 v1, v10, s18, 0
	v_fma_mixlo_f16 v2, v11, s18, 0
	ds_write_b16 v13, v1
	ds_write_b16 v14, v2
	s_and_saveexec_b64 s[12:13], vcc
	v_fma_mixlo_f16 v3, v12, s18, 0
	ds_write_b16 v15, v3
	s_mov_b64 exec, s[12:13]

.LBB0_38:
	s_waitcnt lgkmcnt(0)
	s_load_dwordx2 s[4:5], s[0:1], 0x38
	s_add_i32 s3, s2, 0xfffffc00
	s_movk_i32 s8, 0x240
	s_lshr_b32 s3, s3, 1
	s_and_b32 s16, s2, 1
	v_cmp_gt_u32_e32 vcc, s8, v0
	s_and_saveexec_b64 s[8:9], vcc
	s_cbranch_execz .LBB0_41
	s_load_dwordx2 s[10:11], s[0:1], 0x8
	s_lshl_b32 s12, s3, 7
	s_lshl_b32 s13, s16, 6
	s_or_b32 s12, s12, s13
	s_mul_hi_u32 s13, s12, 36
	s_mul_i32 s12, s12, 36
	v_mov_b32_e32 v3, 0
	s_waitcnt lgkmcnt(0)
	s_add_u32 s10, s10, s12
	v_mov_b32_e32 v1, v3
	s_addc_u32 s11, s11, s13
	s_mov_b64 s[12:13], 0
	s_mov_b32 s17, 0xe38f
	s_mov_b32 s18, 0x42000000
	s_movk_i32 s19, 0x90
	s_mov_b64 s[14:15], 0x100
	s_movk_i32 s20, 0x13f
	v_mov_b64_e32 v[4:5], v[0:1]
	v_lshlrev_b32_e32 v6, 2, v0
	global_load_dword v10, v6, s[10:11] nt
	global_load_dword v11, v6, s[10:11] offset:1024 nt
	v_cmp_gt_u32_e32 vcc, 64, v0
	s_and_saveexec_b64 s[12:13], vcc
	global_load_dword v12, v6, s[10:11] offset:2048 nt
	s_mov_b64 exec, s[12:13]
	s_movk_i32 s14, 0xfaf2
	v_mul_u32_u24_e32 v8, 0xe38f, v0
	v_lshrrev_b32_e32 v8, 19, v8
	v_mul_u32_u24_e32 v9, 0x90, v0
	v_mad_i32_i24 v13, v8, s14, v9
	v_add_u32_e32 v7, 0x100, v0
	v_mul_u32_u24_e32 v8, 0xe38f, v7
	v_lshrrev_b32_e32 v8, 19, v8
	v_mul_u32_u24_e32 v9, 0x90, v7
	v_mad_i32_i24 v14, v8, s14, v9
	v_add_u32_e32 v7, 0x200, v0
	v_mul_u32_u24_e32 v8, 0xe38f, v7
	v_lshrrev_b32_e32 v8, 19, v8
	v_mul_u32_u24_e32 v9, 0x90, v7
	v_mad_i32_i24 v15, v8, s14, v9
	s_waitcnt vmcnt(0)
	v_fma_mixlo_f16 v1, v10, s18, 0
	v_fma_mixlo_f16 v2, v11, s18, 0
	ds_write_b16 v13, v1
	ds_write_b16 v14, v2
	s_and_saveexec_b64 s[12:13], vcc
	v_fma_mixlo_f16 v3, v12, s18, 0
	ds_write_b16 v15, v3
	s_mov_b64 exec, s[12:13]

.LBB0_44:
	s_and_saveexec_b64 s[8:9], s[6:7]
	s_cbranch_execz .LBB0_46
	v_lshlrev_b64 v[8:9], 7, v[8:9]
	s_waitcnt lgkmcnt(0)
	v_lshl_add_u64 v[8:9], s[4:5], 0, v[8:9]
	v_lshl_add_u64 v[6:7], v[6:7], 1, v[8:9]
	global_store_dwordx4 v[6:7], v[2:5], off sc0 sc1

.LBB0_52:
	ds_read_b128 v[6:9], v4
	v_add_u32_e32 v1, 0x100, v1
	v_cmp_lt_u32_e32 vcc, s3, v1
	v_add_u32_e32 v4, 0x1200, v4
	s_or_b64 s[4:5], vcc, s[4:5]
	s_waitcnt lgkmcnt(0)
	global_store_dwordx4 v[2:3], v[6:9], off sc0 sc1
	v_lshl_add_u64 v[2:3], v[2:3], 0, s[8:9]
	s_andn2_b64 exec, exec, s[4:5]
	s_cbranch_execnz .LBB0_52

.LBB0_60:
	ds_read_b128 v[4:7], v3
	v_add_u32_e32 v2, 0x100, v2
	v_cmp_lt_u32_e32 vcc, s4, v2
	v_add_u32_e32 v3, 0x1200, v3
	s_or_b64 s[0:1], vcc, s[0:1]
	s_waitcnt lgkmcnt(0)
	global_store_dwordx4 v[0:1], v[4:7], off sc0 sc1
	v_lshl_add_u64 v[0:1], v[0:1], 0, s[2:3]
	s_andn2_b64 exec, exec, s[0:1]
	s_cbranch_execnz .LBB0_60

_Z6conv_kILi128ELi256ELi3ELi64ELi1ELi1ELb0EEvPKDF16_S1_PKfS3_PDF16_S4_S1_fS3_S3_S3_S3_:
	s_lshl_b32 s3, s2, 3
	s_load_dwordx2 s[20:21], s[0:1], 0x0
	s_load_dwordx4 s[4:7], s[0:1], 0x10
	s_load_dwordx2 s[18:19], s[0:1], 0x30
	s_and_b32 s3, s3, 56
	s_ashr_i32 s8, s2, 5
	s_add_i32 s3, s3, s8
	v_readfirstlane_b32 s27, v0
	s_lshl_b32 s8, s3, 2
	s_bfe_u32 s22, s2, 0x20003
	s_and_b32 s24, s8, 56
	s_lshr_b32 s33, s27, 6
	s_ashr_i32 s25, s3, 4
	s_and_b32 s15, s2, 32
	s_lshl_b32 s2, s22, 8
	v_bfe_u32 v24, v0, 3, 3
	v_and_b32_e32 v2, 7, v0
	s_waitcnt lgkmcnt(0)
	s_add_u32 s2, s4, s2
	v_bitop3_b32 v2, v24, v2, 6 bitop3:0x6c
	s_addc_u32 s3, s5, 0
	v_and_b32_e32 v18, 48, v0
	v_mov_b32_e32 v19, 0
	v_lshlrev_b32_e32 v20, 3, v2
	v_lshl_add_u64 v[2:3], s[2:3], 0, v[18:19]
	s_load_dword s14, s[6:7], 0x0
	global_load_dwordx4 v[14:17], v[2:3], off
	v_lshl_add_u64 v[4:5], v[2:3], 0, 64
	s_mov_b64 s[2:3], 0x80
	global_load_dwordx4 v[10:13], v[4:5], off
	v_lshl_add_u64 v[4:5], v[2:3], 0, s[2:3]
	s_mov_b64 s[2:3], 0xc0
	v_lshl_add_u64 v[2:3], v[2:3], 0, s[2:3]
	v_lshl_or_b32 v18, s33, 3, v24
	s_mov_b32 s2, 0x1e1e1e1f
	v_mul_hi_u32 v21, v18, s2
	v_lshrrev_b32_e32 v21, 2, v21
	s_movk_i32 s4, 0xffde
	s_add_i32 s12, s24, -1
	global_load_dwordx4 v[6:9], v[4:5], off
	v_mul_lo_u32 v22, v21, s4
	v_add_u32_e32 v46, s12, v21
	s_add_i32 s13, s15, -1
	s_movk_i32 s5, 0x154
	global_load_dwordx4 v[2:5], v[2:3], off
	v_add3_u32 v47, s13, v18, v22
	v_cmp_gt_u32_e32 vcc, s5, v18
	v_cmp_gt_u32_e64 s[2:3], 64, v46
	s_and_b64 s[2:3], vcc, s[2:3]
	v_cmp_gt_u32_e32 vcc, 64, v47
	v_and_b32_e32 v1, 63, v0
	s_and_b64 vcc, s[2:3], vcc
	v_mov_b64_e32 v[22:23], s[18:19]
	v_lshlrev_b32_e32 v18, 1, v20
	s_and_saveexec_b64 s[2:3], vcc
	s_lshl_b32 s6, s25, 13
	v_lshlrev_b32_e32 v21, 6, v46
	v_or3_b32 v22, v21, s6, v47
	v_ashrrev_i32_e32 v23, 31, v22
	v_lshlrev_b64 v[22:23], 7, v[22:23]
	v_lshl_add_u64 v[22:23], s[20:21], 0, v[22:23]
	v_lshl_add_u64 v[22:23], v[22:23], 0, v[18:19]
	s_or_b64 exec, exec, s[2:3]
	s_lshl_b32 s36, s33, 10
	v_lshlrev_b32_e32 v21, 4, v1
	v_or_b32_e32 v19, s36, v21
	s_add_i32 s7, s33, 8
	v_readfirstlane_b32 s2, v19
	s_mov_b32 m0, s2
	v_lshl_or_b32 v19, s7, 3, v24
	global_load_lds_dwordx4 v[22:23], off
	s_mov_b32 s6, 0x3c3c3c3d
	v_mul_hi_u32 v22, v19, s6
	v_lshrrev_b32_e32 v22, 3, v22
	v_mul_lo_u32 v23, v22, s4
	v_add_u32_e32 v48, s12, v22
	v_add3_u32 v49, s13, v19, v23
	v_cmp_gt_u32_e64 s[2:3], s5, v19
	v_cmp_gt_u32_e64 s[4:5], 64, v48
	s_and_b64 s[4:5], s[2:3], s[4:5]
	v_cmp_gt_u32_e64 s[2:3], 64, v49
	s_and_b64 s[2:3], s[4:5], s[2:3]
	v_mov_b64_e32 v[22:23], s[18:19]
	s_and_saveexec_b64 s[4:5], s[2:3]
	s_lshl_b32 s8, s25, 13
	v_lshlrev_b32_e32 v19, 6, v48
	v_or3_b32 v22, v19, s8, v49
	v_ashrrev_i32_e32 v23, 31, v22
	v_lshlrev_b64 v[22:23], 7, v[22:23]
	v_lshl_add_u64 v[22:23], s[20:21], 0, v[22:23]
	v_mov_b32_e32 v19, 0
	v_lshl_add_u64 v[22:23], v[22:23], 0, v[18:19]
	s_or_b64 exec, exec, s[4:5]
	s_lshl_b32 s37, s7, 10
	v_or_b32_e32 v19, s37, v21
	s_add_i32 s10, s33, 16
	v_readfirstlane_b32 s4, v19
	s_mov_b32 m0, s4
	v_lshl_or_b32 v19, s10, 3, v24
	global_load_lds_dwordx4 v[22:23], off
	v_mul_hi_u32 v22, v19, s6
	v_lshrrev_b32_e32 v22, 3, v22
	s_movk_i32 s8, 0xffde
	v_mul_lo_u32 v23, v22, s8
	v_add_u32_e32 v58, s12, v22
	s_movk_i32 s9, 0x154
	v_add3_u32 v59, s13, v19, v23
	v_cmp_gt_u32_e64 s[4:5], s9, v19
	v_cmp_gt_u32_e64 s[6:7], 64, v58
	s_and_b64 s[6:7], s[4:5], s[6:7]
	v_cmp_gt_u32_e64 s[4:5], 64, v59
	s_and_b64 s[4:5], s[6:7], s[4:5]
	v_mov_b64_e32 v[22:23], s[18:19]
	s_and_saveexec_b64 s[6:7], s[4:5]
	s_lshl_b32 s11, s25, 13
	v_lshlrev_b32_e32 v19, 6, v58
	v_or3_b32 v22, v19, s11, v59
	v_ashrrev_i32_e32 v23, 31, v22
	v_lshlrev_b64 v[22:23], 7, v[22:23]
	v_lshl_add_u64 v[22:23], s[20:21], 0, v[22:23]
	v_mov_b32_e32 v19, 0
	v_lshl_add_u64 v[22:23], v[22:23], 0, v[18:19]
	s_or_b64 exec, exec, s[6:7]
	s_lshl_b32 s38, s10, 10
	v_or_b32_e32 v19, s38, v21
	s_add_i32 s11, s33, 24
	v_readfirstlane_b32 s6, v19
	s_mov_b32 m0, s6
	v_lshl_or_b32 v19, s11, 3, v24
	global_load_lds_dwordx4 v[22:23], off
	s_mov_b32 s10, 0x3c3c3c3d
	v_mul_hi_u32 v22, v19, s10
	v_lshrrev_b32_e32 v22, 3, v22
	v_mul_lo_u32 v23, v22, s8
	v_add_u32_e32 v60, s12, v22
	v_add3_u32 v61, s13, v19, v23
	v_cmp_gt_u32_e64 s[6:7], s9, v19
	v_cmp_gt_u32_e64 s[8:9], 64, v60
	s_and_b64 s[8:9], s[6:7], s[8:9]
	v_cmp_gt_u32_e64 s[6:7], 64, v61
	s_and_b64 s[6:7], s[8:9], s[6:7]
	v_mov_b64_e32 v[22:23], s[18:19]
	s_and_saveexec_b64 s[8:9], s[6:7]
	s_lshl_b32 s16, s25, 13
	v_lshlrev_b32_e32 v19, 6, v60
	v_or3_b32 v22, v19, s16, v61
	v_ashrrev_i32_e32 v23, 31, v22
	v_lshlrev_b64 v[22:23], 7, v[22:23]
	v_lshl_add_u64 v[22:23], s[20:21], 0, v[22:23]
	v_mov_b32_e32 v19, 0
	v_lshl_add_u64 v[22:23], v[22:23], 0, v[18:19]
	s_or_b64 exec, exec, s[8:9]
	s_lshl_b32 s39, s11, 10
	v_or_b32_e32 v19, s39, v21
	s_add_i32 s16, s33, 32
	v_readfirstlane_b32 s8, v19
	s_mov_b32 m0, s8
	v_lshl_or_b32 v19, s16, 3, v24
	global_load_lds_dwordx4 v[22:23], off
	v_mul_hi_u32 v22, v19, s10
	v_lshrrev_b32_e32 v22, 3, v22
	s_movk_i32 s8, 0xffde
	v_mul_lo_u32 v23, v22, s8
	v_add_u32_e32 v62, s12, v22
	s_movk_i32 s8, 0x154
	v_add3_u32 v63, s13, v19, v23
	v_cmp_gt_u32_e64 s[8:9], s8, v19
	v_cmp_gt_u32_e64 s[10:11], 64, v62
	s_and_b64 s[10:11], s[8:9], s[10:11]
	v_cmp_gt_u32_e64 s[8:9], 64, v63
	s_and_b64 s[8:9], s[10:11], s[8:9]
	s_xor_b64 s[10:11], s[8:9], -1
	s_and_saveexec_b64 s[28:29], s[10:11]
	s_xor_b64 s[10:11], exec, s[28:29]
	s_lshl_b32 s17, s25, 13
	s_or_saveexec_b64 s[10:11], s[10:11]
	v_mov_b32_e32 v64, s17
	v_mov_b64_e32 v[22:23], s[18:19]
	s_xor_b64 exec, exec, s[10:11]
	s_lshl_b32 s17, s25, 13
	v_lshlrev_b32_e32 v19, 6, v62
	v_or3_b32 v22, v19, s17, v63
	v_ashrrev_i32_e32 v23, 31, v22
	v_lshlrev_b64 v[22:23], 7, v[22:23]
	v_lshl_add_u64 v[22:23], s[20:21], 0, v[22:23]
	v_mov_b32_e32 v19, 0
	v_lshl_add_u64 v[22:23], v[22:23], 0, v[18:19]
	v_mov_b32_e32 v64, s17
	s_or_b64 exec, exec, s[10:11]
	s_lshl_b32 s40, s16, 10
	v_or_b32_e32 v18, s40, v21
	s_add_i32 s23, s33, 40
	v_readfirstlane_b32 s10, v18
	s_mov_b32 m0, s10
	v_lshl_or_b32 v19, s23, 3, v24
	global_load_lds_dwordx4 v[22:23], off
	s_mov_b32 s10, 0x3c3c3c3d
	v_mul_hi_u32 v18, v19, s10
	v_lshrrev_b32_e32 v18, 3, v18
	s_movk_i32 s10, 0xffde
	s_load_dwordx2 s[16:17], s[0:1], 0x8
	v_mul_lo_u32 v22, v18, s10
	v_add_u32_e32 v18, s12, v18
	s_movk_i32 s10, 0x154
	v_add3_u32 v65, s13, v19, v22
	v_cmp_gt_u32_e64 s[10:11], s10, v19
	v_cmp_gt_u32_e64 s[12:13], 64, v18
	s_and_b64 s[12:13], s[10:11], s[12:13]
	v_cmp_gt_u32_e64 s[10:11], 64, v65
	s_and_b64 s[10:11], s[12:13], s[10:11]
	s_xor_b64 s[12:13], s[10:11], -1
	v_lshlrev_b32_e32 v66, 6, v18
	s_and_saveexec_b64 s[28:29], s[12:13]
	s_xor_b64 s[12:13], exec, s[28:29]
	v_lshlrev_b32_e32 v66, 6, v18
	s_or_saveexec_b64 s[12:13], s[12:13]
	v_mov_b64_e32 v[18:19], s[18:19]
	s_xor_b64 exec, exec, s[12:13]
	v_or3_b32 v18, v66, v64, v65
	v_ashrrev_i32_e32 v19, 31, v18
	v_lshlrev_b64 v[18:19], 7, v[18:19]
	v_lshl_add_u64 v[18:19], s[20:21], 0, v[18:19]
	v_lshlrev_b32_e32 v22, 1, v20
	v_mov_b32_e32 v23, 0
	v_lshl_add_u64 v[18:19], v[18:19], 0, v[22:23]
	s_or_b64 exec, exec, s[12:13]
	v_lshrrev_b32_e32 v129, 4, v1
	v_bitop3_b32 v23, v129, v0, 6 bitop3:0x78
	v_and_b32_e32 v128, 15, v0
	v_lshlrev_b32_e32 v23, 4, v23
	s_lshr_b32 s29, s27, 8
	v_lshl_or_b32 v23, v128, 7, v23
	v_lshl_or_b32 v23, s29, 13, v23
	s_lshl_b32 s41, s23, 10
	s_lshl_b32 s26, s22, 6
	s_and_b32 s28, s33, 3
	v_add_u32_e32 v132, 0x18000, v23
	v_or_b32_e32 v23, s41, v21
	s_lshl_b32 s22, s22, 13
	v_readfirstlane_b32 s23, v23
	s_waitcnt lgkmcnt(0)
	s_add_u32 s22, s16, s22
	s_mul_hi_u32 s44, s27, 0x38e38e39
	s_mov_b32 m0, s23
	s_addc_u32 s23, s17, 0
	s_lshr_b32 s16, s44, 10
	s_mul_i32 s16, s16, -9
	s_add_i32 s16, s16, s29
	s_lshl_b32 s34, s33, 11
	s_ashr_i32 s17, s16, 31
	s_add_i32 s33, s34, 0x18000
	s_lshl_b64 s[16:17], s[16:17], 15
	s_add_u32 s16, s22, s16
	s_addc_u32 s17, s23, s17
	s_add_i32 s42, s29, 2
	s_mul_hi_u32 s43, s42, 0xe38e38f
	v_lshl_or_b32 v22, v24, 6, s36
	s_movk_i32 s31, 0xdc0
	s_mul_i32 s43, s43, -9
	v_and_or_b32 v22, v22, s31, v20
	s_add_i32 s42, s43, s42
	global_load_lds_dwordx4 v[18:19], off
	v_lshlrev_b32_e32 v18, 1, v22
	v_mov_b32_e32 v19, 0
	s_mov_b32 m0, s33
	s_ashr_i32 s43, s42, 31
	v_lshl_add_u64 v[22:23], s[16:17], 0, v[18:19]
	global_load_lds_dwordx4 v18, s[16:17]
	s_mov_b64 s[16:17], 0x400
	s_add_i32 m0, s34, 0x18400
	s_lshl_b64 s[42:43], s[42:43], 15
	v_lshl_add_u64 v[22:23], v[22:23], 0, s[16:17]
	s_add_u32 s42, s22, s42
	global_load_lds_dwordx4 v[22:23], off
	s_addc_u32 s43, s23, s43
	s_add_i32 m0, s34, 0x1c000
	v_lshl_add_u64 v[22:23], s[42:43], 0, v[18:19]
	global_load_lds_dwordx4 v18, s[42:43]
	s_add_i32 s42, s29, 4
	s_mul_hi_u32 s43, s42, 0xe38e38f
	s_mul_i32 s43, s43, -9
	s_add_i32 s42, s43, s42
	s_ashr_i32 s43, s42, 31
	s_add_i32 m0, s34, 0x1c400
	s_lshl_b64 s[42:43], s[42:43], 15
	s_add_u32 s42, s22, s42
	v_lshl_add_u64 v[22:23], v[22:23], 0, s[16:17]
	s_addc_u32 s43, s23, s43
	global_load_lds_dwordx4 v[22:23], off
	s_add_i32 m0, s34, 0x20000
	v_lshl_add_u64 v[22:23], s[42:43], 0, v[18:19]
	global_load_lds_dwordx4 v18, s[42:43]
	v_lshl_add_u64 v[22:23], v[22:23], 0, s[16:17]
	s_add_i32 m0, s34, 0x20400
	s_lshr_b32 s34, s44, 9
	global_load_lds_dwordx4 v[22:23], off
	s_mul_i32 s34, s34, -9
	s_add_i32 s34, s34, s29
	s_mul_hi_i32 s42, s34, 0x55555556
	s_lshr_b32 s43, s42, 31
	s_mul_i32 s31, s28, 0x44
	s_add_i32 s42, s42, s43
	v_add_u32_e32 v130, s31, v128
	s_mul_i32 s42, s42, 31
	v_add_u32_e32 v131, 34, v130
	s_add_i32 s42, s42, s34
	s_bitcmp1_b32 s44, 9
	v_add_u32_e32 v30, s42, v130
	v_add_u32_e32 v38, s42, v131
	s_movk_i32 s42, 0x1000
	v_lshlrev_b32_e32 v68, 1, v20
	v_lshl_add_u32 v20, v48, 6, v64
	s_waitcnt vmcnt(4) lgkmcnt(0)
	s_barrier
	s_cselect_b32 s43, 0xc000, 0
	ds_read_b128 v[26:29], v132
	v_add3_u32 v48, v20, v49, s42
	v_lshl_add_u32 v20, v58, 6, v64
	ds_read_b128 v[22:25], v132 offset:2048
	v_bitop3_b32 v31, v30, v129, 6 bitop3:0x6c
	v_lshl_add_u32 v30, v30, 7, s43
	v_add3_u32 v58, v20, v59, s42
	v_lshl_add_u32 v20, v60, 6, v64
	v_lshl_or_b32 v134, v31, 4, v30
	ds_read_b128 v[34:37], v134
	v_lshl_add_u32 v46, v46, 6, v64
	v_add3_u32 v60, v20, v61, s42
	v_lshl_add_u32 v20, v62, 6, v64
	ds_read_b128 v[30:33], v134 offset:2048
	v_bitop3_b32 v39, v38, v129, 6 bitop3:0x6c
	v_lshl_add_u32 v38, v38, 7, s43
	v_add3_u32 v46, v46, v47, s42
	v_add3_u32 v62, v20, v63, s42
	v_add_u32_e32 v20, v66, v64
	v_lshl_add_u64 v[126:127], s[22:23], 0, v[18:19]
	v_add_u32_e32 v18, s36, v21
	v_lshl_or_b32 v135, v39, 4, v38
	ds_read_b128 v[42:45], v135
	v_ashrrev_i32_e32 v47, 31, v46
	v_add3_u32 v64, v20, v65, s42
	v_add_u32_e32 v136, 0xc000, v18
	v_add_u32_e32 v18, s37, v21
	s_load_dwordx2 s[12:13], s[0:1], 0x20
	ds_read_b128 v[38:41], v135 offset:2048
	v_lshlrev_b64 v[46:47], 7, v[46:47]
	v_ashrrev_i32_e32 v49, 31, v48
	v_ashrrev_i32_e32 v59, 31, v58
	v_ashrrev_i32_e32 v61, 31, v60
	v_ashrrev_i32_e32 v63, 31, v62
	v_ashrrev_i32_e32 v65, 31, v64
	v_add_u32_e32 v137, 0xc000, v18
	v_add_u32_e32 v18, s38, v21
	ds_read_b128 v[54:57], v132 offset:4096
	v_lshl_add_u64 v[46:47], s[20:21], 0, v[46:47]
	v_mov_b32_e32 v69, v19
	v_lshlrev_b64 v[48:49], 7, v[48:49]
	v_lshlrev_b64 v[58:59], 7, v[58:59]
	v_lshlrev_b64 v[60:61], 7, v[60:61]
	v_lshlrev_b64 v[62:63], 7, v[62:63]
	v_lshlrev_b64 v[64:65], 7, v[64:65]
	v_add_u32_e32 v138, 0xc000, v18
	v_add_u32_e32 v18, s39, v21
	ds_read_b128 v[50:53], v132 offset:6144
	v_lshl_add_u64 v[46:47], v[46:47], 0, v[68:69]
	v_lshl_add_u64 v[48:49], s[20:21], 0, v[48:49]
	v_lshl_add_u64 v[58:59], s[20:21], 0, v[58:59]
	v_lshl_add_u64 v[60:61], s[20:21], 0, v[60:61]
	v_lshl_add_u64 v[62:63], s[20:21], 0, v[62:63]
	v_lshl_add_u64 v[64:65], s[20:21], 0, v[64:65]
	v_mov_b32_e32 v20, s19
	v_add_u32_e32 v139, 0xc000, v18
	v_add_u32_e32 v18, s40, v21
	v_lshl_add_u64 v[48:49], v[48:49], 0, v[68:69]
	v_lshl_add_u64 v[58:59], v[58:59], 0, v[68:69]
	v_lshl_add_u64 v[60:61], v[60:61], 0, v[68:69]
	v_lshl_add_u64 v[62:63], v[62:63], 0, v[68:69]
	v_lshl_add_u64 v[64:65], v[64:65], 0, v[68:69]
	v_cndmask_b32_e32 v115, v20, v47, vcc
	v_mov_b32_e32 v47, s18
	v_add_u32_e32 v140, 0xc000, v18
	v_add_u32_e32 v18, s41, v21
	s_mov_b32 s30, 6
	v_xor_b32_e32 v133, 64, v132
	s_mov_b32 s31, 0
	s_mov_b32 s35, 1
	s_mov_b32 s34, 0xc000
	v_cndmask_b32_e32 v114, v47, v46, vcc
	v_cndmask_b32_e64 v117, v20, v49, s[2:3]
	v_cndmask_b32_e64 v116, v47, v48, s[2:3]
	v_cndmask_b32_e64 v119, v20, v59, s[4:5]
	v_cndmask_b32_e64 v118, v47, v58, s[4:5]
	v_cndmask_b32_e64 v121, v20, v61, s[6:7]
	v_cndmask_b32_e64 v120, v47, v60, s[6:7]
	v_cndmask_b32_e64 v123, v20, v63, s[8:9]
	v_cndmask_b32_e64 v122, v47, v62, s[8:9]
	v_cndmask_b32_e64 v125, v20, v65, s[10:11]
	v_cndmask_b32_e64 v124, v47, v64, s[10:11]
	s_mov_b64 s[2:3], 0
	v_add_u32_e32 v141, 0xc000, v18
	v_mov_b32_e32 v18, v19
	v_mov_b32_e32 v20, v19
	v_mov_b32_e32 v21, v19
	v_mov_b32_e32 v46, v19
	v_mov_b32_e32 v47, v19
	v_mov_b32_e32 v48, v19
	v_mov_b32_e32 v49, v19
	v_mov_b32_e32 v58, v19
	v_mov_b32_e32 v59, v19
	v_mov_b32_e32 v60, v19
	v_mov_b32_e32 v61, v19
	v_mov_b32_e32 v74, v19
	v_mov_b32_e32 v75, v19
	v_mov_b32_e32 v76, v19
	v_mov_b32_e32 v77, v19
	v_mov_b32_e32 v82, v19
	v_mov_b32_e32 v83, v19
	v_mov_b32_e32 v84, v19
	v_mov_b32_e32 v85, v19
	v_mov_b32_e32 v86, v19
	v_mov_b32_e32 v87, v19
	v_mov_b32_e32 v88, v19
	v_mov_b32_e32 v89, v19
	v_mov_b32_e32 v90, v19
	v_mov_b32_e32 v91, v19
	v_mov_b32_e32 v92, v19
	v_mov_b32_e32 v93, v19
	v_mov_b32_e32 v94, v19
	v_mov_b32_e32 v95, v19
	v_mov_b32_e32 v96, v19
	v_mov_b32_e32 v97, v19
	v_mov_b32_e32 v98, v19
	v_mov_b32_e32 v99, v19
	v_mov_b32_e32 v100, v19
	v_mov_b32_e32 v101, v19
	v_mov_b32_e32 v102, v19
	v_mov_b32_e32 v103, v19
	v_mov_b32_e32 v104, v19
	v_mov_b32_e32 v105, v19
	v_mov_b32_e32 v106, v19
	v_mov_b32_e32 v107, v19
	v_mov_b32_e32 v108, v19
	v_mov_b32_e32 v109, v19
	v_mov_b32_e32 v110, v19
	v_mov_b32_e32 v111, v19
	v_mov_b32_e32 v112, v19
	v_mov_b32_e32 v113, v19
	v_mov_b32_e32 v78, v19
	v_mov_b32_e32 v79, v19
	v_mov_b32_e32 v80, v19
	v_mov_b32_e32 v81, v19
	v_mov_b32_e32 v62, v19
	v_mov_b32_e32 v63, v19
	v_mov_b32_e32 v64, v19
	v_mov_b32_e32 v65, v19
	v_mov_b32_e32 v70, v19
	v_mov_b32_e32 v71, v19
	v_mov_b32_e32 v72, v19
	v_mov_b32_e32 v73, v19
	v_mov_b32_e32 v66, v19
	v_mov_b32_e32 v67, v19
	v_mov_b32_e32 v68, v19
	s_mov_b32 s60, 0
	s_add_i32 s63, s29, 2
	s_mul_i32 s73, s63, 11
	s_lshr_b32 s73, s73, 5
	s_mul_i32 s73, s73, 31
	s_add_i32 s62, s63, s73
	s_mov_b32 s64, 0
	s_mov_b32 s66, 1
	s_mov_b32 s67, 0
	s_add_i32 s75, s29, 6
	s_lshl_b32 s68, s75, 15
	s_mov_b32 s69, 0
	v_lshl_add_u64 v[178:179], v[126:127], 0, s[68:69]
	s_add_i32 s70, s33, 0xc000
	v_lshl_add_u64 v[180:181], v[178:179], 0, s[16:17]
	v_mov_b32_e32 v174, v133

.Lc2_bar:
	s_barrier
	s_waitcnt lgkmcnt(5)
	v_mfma_f32_16x16x32_f16 v[110:113], v[26:29], v[34:37], v[110:113]
	ds_read_b128 v[142:145], v174
	v_mfma_f32_16x16x32_f16 v[106:109], v[22:25], v[34:37], v[106:109]
	v_xor_b32_e32 v176, 64, v134
	s_waitcnt lgkmcnt(5)
	v_mfma_f32_16x16x32_f16 v[94:97], v[26:29], v[30:33], v[94:97]
	ds_read_b128 v[146:149], v174 offset:2048
	v_mfma_f32_16x16x32_f16 v[90:93], v[22:25], v[30:33], v[90:93]
	v_xor_b32_e32 v177, 64, v135
	s_mov_b32 m0, s70
	s_add_i32 s71, s34, 0xffff8000
	global_load_lds_dwordx4 v[178:179], off
	s_waitcnt lgkmcnt(5)
	v_mfma_f32_16x16x32_f16 v[74:77], v[26:29], v[42:45], v[74:77]
	ds_read_b128 v[150:153], v176
	v_mfma_f32_16x16x32_f16 v[58:61], v[22:25], v[42:45], v[58:61]
	s_and_b32 s71, s71, 0xc000
	s_add_i32 s72, s70, 0x400
	s_waitcnt lgkmcnt(5)
	v_mfma_f32_16x16x32_f16 v[78:81], v[26:29], v[38:41], v[78:81]
	ds_read_b128 v[154:157], v176 offset:2048
	v_mfma_f32_16x16x32_f16 v[62:65], v[22:25], v[38:41], v[62:65]
	v_add_u32_e32 v175, s71, v132
	s_waitcnt lgkmcnt(5)
	v_mfma_f32_16x16x32_f16 v[102:105], v[54:57], v[34:37], v[102:105]
	ds_read_b128 v[158:161], v177
	s_waitcnt lgkmcnt(5)
	v_mfma_f32_16x16x32_f16 v[98:101], v[50:53], v[34:37], v[98:101]
	v_mfma_f32_16x16x32_f16 v[86:89], v[54:57], v[30:33], v[86:89]
	ds_read_b128 v[162:165], v177 offset:2048
	v_mfma_f32_16x16x32_f16 v[82:85], v[50:53], v[30:33], v[82:85]
	v_add_u32_e32 v182, s62, v130
	v_mfma_f32_16x16x32_f16 v[46:49], v[54:57], v[42:45], v[46:49]
	ds_read_b128 v[166:169], v174 offset:4096
	v_mfma_f32_16x16x32_f16 v[18:21], v[50:53], v[42:45], v[18:21]
	v_bitop3_b32 v183, v182, v129, 6 bitop3:0x6c
	v_lshl_add_u32 v182, v182, 7, s64
	v_mfma_f32_16x16x32_f16 v[70:73], v[54:57], v[38:41], v[70:73]
	ds_read_b128 v[170:173], v174 offset:6144
	v_mfma_f32_16x16x32_f16 v[66:69], v[50:53], v[38:41], v[66:69]
	v_lshl_or_b32 v134, v183, 4, v182
	v_add_u32_e32 v174, s71, v133
	s_waitcnt lgkmcnt(5)
	v_mfma_f32_16x16x32_f16 v[110:113], v[142:145], v[150:153], v[110:113]
	ds_read_b128 v[26:29], v175
	v_mfma_f32_16x16x32_f16 v[106:109], v[146:149], v[150:153], v[106:109]
	s_mov_b32 m0, s72
	s_add_i32 s63, s63, 2
	global_load_lds_dwordx4 v[180:181], off
	s_waitcnt lgkmcnt(5)
	v_mfma_f32_16x16x32_f16 v[94:97], v[142:145], v[154:157], v[94:97]
	ds_read_b128 v[22:25], v175 offset:2048
	v_mfma_f32_16x16x32_f16 v[90:93], v[146:149], v[154:157], v[90:93]
	v_add_u32_e32 v182, s62, v131
	s_waitcnt lgkmcnt(5)
	v_mfma_f32_16x16x32_f16 v[74:77], v[142:145], v[158:161], v[74:77]
	ds_read_b128 v[34:37], v134
	v_mfma_f32_16x16x32_f16 v[58:61], v[146:149], v[158:161], v[58:61]
	v_bitop3_b32 v183, v182, v129, 6 bitop3:0x6c
	v_lshl_add_u32 v182, v182, 7, s64
	s_waitcnt lgkmcnt(5)
	v_mfma_f32_16x16x32_f16 v[78:81], v[142:145], v[162:165], v[78:81]
	ds_read_b128 v[30:33], v134 offset:2048
	v_mfma_f32_16x16x32_f16 v[62:65], v[146:149], v[162:165], v[62:65]
	v_lshl_or_b32 v135, v183, 4, v182
	s_waitcnt lgkmcnt(5)
	v_mfma_f32_16x16x32_f16 v[102:105], v[166:169], v[150:153], v[102:105]
	ds_read_b128 v[42:45], v135
	s_waitcnt lgkmcnt(5)
	v_mfma_f32_16x16x32_f16 v[98:101], v[170:173], v[150:153], v[98:101]
	s_cmp_ge_u32 s63, 9
	s_cselect_b32 s73, 9, 0
	s_cselect_b32 s74, 0xc000, 0
	s_sub_i32 s63, s63, s73
	s_xor_b32 s64, s64, s74
	v_mfma_f32_16x16x32_f16 v[86:89], v[166:169], v[154:157], v[86:89]
	ds_read_b128 v[38:41], v135 offset:2048
	s_mul_i32 s73, s63, 11
	s_lshr_b32 s73, s73, 5
	s_mul_i32 s73, s73, 31
	s_add_i32 s62, s63, s73
	v_mfma_f32_16x16x32_f16 v[82:85], v[170:173], v[154:157], v[82:85]
	s_addk_i32 s34, 0x4000
	s_add_i32 s60, s60, 1
	s_add_i32 s75, s60, 3
	s_cmp_lt_u32 s60, 6
	s_cselect_b32 s75, s75, 8
	s_lshl_b32 s75, s75, 1
	s_add_i32 s75, s75, s29
	s_lshl_b32 s68, s75, 15
	v_mfma_f32_16x16x32_f16 v[46:49], v[166:169], v[158:161], v[46:49]
	ds_read_b128 v[54:57], v175 offset:4096
	v_mfma_f32_16x16x32_f16 v[18:21], v[170:173], v[158:161], v[18:21]
	v_lshl_add_u64 v[178:179], v[126:127], 0, s[68:69]
	s_and_b32 s70, s34, 0xc000
	s_add_i32 s70, s70, s33
	v_mfma_f32_16x16x32_f16 v[70:73], v[166:169], v[162:165], v[70:73]
	ds_read_b128 v[50:53], v175 offset:6144
	v_lshl_add_u64 v[180:181], v[178:179], 0, s[16:17]
	v_mfma_f32_16x16x32_f16 v[66:69], v[170:173], v[162:165], v[66:69]
	s_cmp_lg_u32 s60, s66
	s_cbranch_scc1 .Lc2_nopatch
	v_readfirstlane_b32 s2, v136
	s_mov_b32 m0, s2
	v_readfirstlane_b32 s2, v137
	global_load_lds_dwordx4 v[114:115], off
	s_mov_b32 m0, s2
	v_readfirstlane_b32 s2, v138
	global_load_lds_dwordx4 v[116:117], off
	s_mov_b32 m0, s2
	v_readfirstlane_b32 s2, v139
	global_load_lds_dwordx4 v[118:119], off
	s_mov_b32 m0, s2
	v_readfirstlane_b32 s2, v140
	global_load_lds_dwordx4 v[120:121], off
	s_mov_b32 m0, s2
	v_readfirstlane_b32 s2, v141
	global_load_lds_dwordx4 v[122:123], off
	s_mov_b32 m0, s2
	s_mov_b64 s[2:3], -1
	global_load_lds_dwordx4 v[124:125], off
	s_movk_i32 s66, 0x3e8
	s_mov_b32 s67, 2
.Lc2_nopatch:
	s_cmp_eq_u32 s60, 9
	s_cbranch_scc0 .Lc2_loop

	.amdhsa_kernel _Z6conv_kILi128ELi256ELi3ELi64ELi1ELi1ELb0EEvPKDF16_S1_PKfS3_PDF16_S4_S1_fS3_S3_S3_S3_
		.amdhsa_group_segment_fixed_size 163840
		.amdhsa_private_segment_fixed_size 0
		.amdhsa_kernarg_size 96
		.amdhsa_user_sgpr_count 2
		.amdhsa_user_sgpr_dispatch_ptr 0
		.amdhsa_user_sgpr_queue_ptr 0
		.amdhsa_user_sgpr_kernarg_segment_ptr 1
		.amdhsa_user_sgpr_dispatch_id 0
		.amdhsa_user_sgpr_kernarg_preload_length 0
		.amdhsa_user_sgpr_kernarg_preload_offset 0
		.amdhsa_user_sgpr_private_segment_size 0
		.amdhsa_uses_dynamic_stack 0
		.amdhsa_enable_private_segment 0
		.amdhsa_system_sgpr_workgroup_id_x 1
		.amdhsa_system_sgpr_workgroup_id_y 0
		.amdhsa_system_sgpr_workgroup_id_z 0
		.amdhsa_system_sgpr_workgroup_info 0
		.amdhsa_system_vgpr_workitem_id 0
		.amdhsa_next_free_vgpr 184
		.amdhsa_next_free_sgpr 96
		.amdhsa_accum_offset 184
		.amdhsa_reserve_vcc 1
		.amdhsa_float_round_mode_32 0
		.amdhsa_float_round_mode_16_64 0
		.amdhsa_float_denorm_mode_32 3
		.amdhsa_float_denorm_mode_16_64 3
		.amdhsa_dx10_clamp 1
		.amdhsa_ieee_mode 1
		.amdhsa_fp16_overflow 0
		.amdhsa_tg_split 0
		.amdhsa_exception_fp_ieee_invalid_op 0
		.amdhsa_exception_fp_denorm_src 0
		.amdhsa_exception_fp_ieee_div_zero 0
		.amdhsa_exception_fp_ieee_overflow 0
		.amdhsa_exception_fp_ieee_underflow 0
		.amdhsa_exception_fp_ieee_inexact 0
		.amdhsa_exception_int_div_zero 0
	.end_amdhsa_kernel

.LBB8_14:
	s_or_b64 exec, exec, s[22:23]
	v_lshrrev_b32_e32 v114, 4, v112
	v_bitop3_b32 v7, v114, v0, 6 bitop3:0x78
	v_and_b32_e32 v113, 15, v0
	v_lshlrev_b32_e32 v7, 4, v7
	s_lshr_b32 s23, s28, 8
	v_lshl_or_b32 v7, v113, 7, v7
	v_lshl_or_b32 v6, v8, 6, s37
	s_movk_i32 s22, 0xdc0
	s_and_b32 s30, s3, 3
	v_lshl_or_b32 v7, s23, 13, v7
	s_lshl_b32 s43, s33, 10
	v_and_or_b32 v6, v6, s22, v4
	s_bfe_u32 s22, s2, 0x10003
	s_mul_i32 s2, s30, 0x44
	v_add_u32_e32 v117, 0x18000, v7
	v_or_b32_e32 v7, s43, v5
	v_add_u32_e32 v115, s2, v113
	v_readfirstlane_b32 s2, v7
	s_lshl_b32 s31, s27, 1
	s_mov_b32 m0, s2
	s_lshl_b32 s2, s22, 13
	s_waitcnt lgkmcnt(0)
	s_add_u32 s20, s20, s2
	s_mul_hi_u32 s46, s28, 0x38e38e39
	s_addc_u32 s21, s21, 0
	s_lshr_b32 s47, s46, 9
	s_add_i32 s2, s47, s31
	s_lshl_b32 s35, s3, 11
	s_lshr_b32 s3, s2, 2
	s_add_i32 s3, s3, s31
	s_and_b32 s2, s2, 0x3ffffc
	s_sub_i32 s2, s3, s2
	s_mul_i32 s2, s2, 9
	s_add_i32 s2, s2, s23
	s_ashr_i32 s3, s2, 31
	s_add_i32 s34, s35, 0x18000
	s_lshl_b64 s[2:3], s[2:3], 14
	s_add_u32 s2, s20, s2
	s_addc_u32 s3, s21, s3
	s_add_i32 s44, s23, 2
	s_mul_hi_u32 s45, s44, 0x1c71c71d
	s_add_i32 s45, s45, s31
	s_lshr_b32 s48, s45, 2
	s_add_i32 s48, s48, s31
	s_and_b32 s45, s45, 0x7ffffc
	s_sub_i32 s45, s48, s45
	s_mul_i32 s45, s45, 9
	s_add_i32 s44, s45, s44
	global_load_lds_dwordx4 v[2:3], off
	v_lshlrev_b32_e32 v2, 1, v6
	v_mov_b32_e32 v3, 0
	s_mov_b32 m0, s34
	s_ashr_i32 s45, s44, 31
	v_lshl_add_u64 v[6:7], s[2:3], 0, v[2:3]
	global_load_lds_dwordx4 v2, s[2:3]
	s_mov_b64 s[2:3], 0x400
	s_add_i32 m0, s35, 0x18400
	s_lshl_b64 s[44:45], s[44:45], 14
	v_lshl_add_u64 v[6:7], v[6:7], 0, s[2:3]
	s_add_u32 s44, s20, s44
	global_load_lds_dwordx4 v[6:7], off
	s_addc_u32 s45, s21, s45
	s_add_i32 m0, s35, 0x1c000
	v_lshl_add_u64 v[6:7], s[44:45], 0, v[2:3]
	global_load_lds_dwordx4 v2, s[44:45]
	s_add_i32 s44, s23, 4
	s_mul_hi_u32 s45, s44, 0x1c71c71d
	s_add_i32 s45, s45, s31
	s_lshr_b32 s48, s45, 2
	s_add_i32 s48, s48, s31
	s_and_b32 s45, s45, 0x7ffffc
	s_sub_i32 s45, s48, s45
	s_mul_i32 s45, s45, 9
	s_add_i32 s44, s45, s44
	s_ashr_i32 s45, s44, 31
	s_add_i32 m0, s35, 0x1c400
	s_lshl_b64 s[44:45], s[44:45], 14
	s_add_u32 s44, s20, s44
	v_lshl_add_u64 v[6:7], v[6:7], 0, s[2:3]
	s_addc_u32 s45, s21, s45
	global_load_lds_dwordx4 v[6:7], off
	s_add_i32 m0, s35, 0x20000
	v_lshl_add_u64 v[6:7], s[44:45], 0, v[2:3]
	global_load_lds_dwordx4 v2, s[44:45]
	v_lshl_add_u64 v[6:7], v[6:7], 0, s[2:3]
	s_add_i32 m0, s35, 0x20400
	s_mul_i32 s35, s47, -9
	global_load_lds_dwordx4 v[6:7], off
	s_add_i32 s35, s35, s23
	s_mul_hi_i32 s44, s35, 0x55555556
	s_lshr_b32 s45, s44, 31
	s_add_i32 s44, s44, s45
	s_mul_i32 s44, s44, 31
	s_add_i32 s44, s44, s35
	s_bitcmp1_b32 s46, 9
	s_cselect_b32 s45, 0xc000, 0
	s_or_b32 s39, s39, 64
	v_lshlrev_b32_e32 v52, 1, v4
	v_add_lshl_u32 v4, v32, s39, 6
	s_waitcnt vmcnt(4) lgkmcnt(0)
	s_barrier
	ds_read_b128 v[10:13], v117
	v_add_u32_e32 v14, s44, v115
	v_add3_u32 v32, v4, v50, v33
	v_add_lshl_u32 v4, v42, s39, 6
	v_add_u32_e32 v116, 34, v115
	ds_read_b128 v[6:9], v117 offset:2048
	v_bitop3_b32 v15, v14, v114, 6 bitop3:0x6c
	v_lshl_add_u32 v14, v14, 7, s45
	v_add3_u32 v42, v4, v50, v43
	v_add_lshl_u32 v4, v44, s39, 6
	v_lshl_or_b32 v119, v15, 4, v14
	ds_read_b128 v[18:21], v119
	v_add_u32_e32 v22, s44, v116
	v_add_lshl_u32 v30, v30, s39, 6
	v_add3_u32 v44, v4, v50, v45
	v_add_lshl_u32 v4, v46, s39, 6
	ds_read_b128 v[14:17], v119 offset:2048
	v_bitop3_b32 v23, v22, v114, 6 bitop3:0x6c
	v_lshl_add_u32 v22, v22, 7, s45
	v_add3_u32 v30, v30, v50, v31
	v_add3_u32 v46, v4, v50, v47
	v_add_lshl_u32 v4, v48, s39, 6
	v_lshl_add_u64 v[110:111], s[20:21], 0, v[2:3]
	v_add_u32_e32 v2, s37, v5
	v_lshl_or_b32 v120, v23, 4, v22
	ds_read_b128 v[26:29], v120
	v_ashrrev_i32_e32 v31, 31, v30
	v_add3_u32 v48, v4, v50, v49
	v_add_u32_e32 v121, 0xc000, v2
	v_add_u32_e32 v2, s38, v5
	ds_read_b128 v[22:25], v120 offset:2048
	v_lshlrev_b64 v[30:31], 7, v[30:31]
	v_ashrrev_i32_e32 v33, 31, v32
	v_ashrrev_i32_e32 v43, 31, v42
	v_ashrrev_i32_e32 v45, 31, v44
	v_ashrrev_i32_e32 v47, 31, v46
	v_ashrrev_i32_e32 v49, 31, v48
	v_add_u32_e32 v122, 0xc000, v2
	v_add_u32_e32 v2, s40, v5
	ds_read_b128 v[38:41], v117 offset:4096
	v_lshl_add_u64 v[30:31], s[18:19], 0, v[30:31]
	v_mov_b32_e32 v53, v3
	v_lshlrev_b64 v[32:33], 7, v[32:33]
	v_lshlrev_b64 v[42:43], 7, v[42:43]
	v_lshlrev_b64 v[44:45], 7, v[44:45]
	v_lshlrev_b64 v[46:47], 7, v[46:47]
	v_lshlrev_b64 v[48:49], 7, v[48:49]
	v_add_u32_e32 v123, 0xc000, v2
	v_add_u32_e32 v2, s41, v5
	ds_read_b128 v[34:37], v117 offset:6144
	v_lshl_add_u64 v[30:31], v[30:31], 0, v[52:53]
	v_lshl_add_u64 v[32:33], s[18:19], 0, v[32:33]
	v_lshl_add_u64 v[42:43], s[18:19], 0, v[42:43]
	v_lshl_add_u64 v[44:45], s[18:19], 0, v[44:45]
	v_lshl_add_u64 v[46:47], s[18:19], 0, v[46:47]
	v_lshl_add_u64 v[48:49], s[18:19], 0, v[48:49]
	v_mov_b32_e32 v4, s17
	v_add_u32_e32 v124, 0xc000, v2
	v_add_u32_e32 v2, s42, v5
	v_lshl_add_u64 v[32:33], v[32:33], 0, v[52:53]
	v_lshl_add_u64 v[42:43], v[42:43], 0, v[52:53]
	v_lshl_add_u64 v[44:45], v[44:45], 0, v[52:53]
	v_lshl_add_u64 v[46:47], v[46:47], 0, v[52:53]
	v_lshl_add_u64 v[48:49], v[48:49], 0, v[52:53]
	v_cndmask_b32_e32 v99, v4, v31, vcc
	v_mov_b32_e32 v31, s16
	v_add_u32_e32 v125, 0xc000, v2
	v_add_u32_e32 v2, s43, v5
	s_mov_b32 s29, 6
	v_xor_b32_e32 v118, 64, v117
	s_mov_b32 s36, 1
	s_mov_b32 s33, 0
	s_mov_b32 s35, 0xc000
	v_cndmask_b32_e32 v98, v31, v30, vcc
	v_cndmask_b32_e64 v101, v4, v33, s[12:13]
	v_cndmask_b32_e64 v100, v31, v32, s[12:13]
	v_cndmask_b32_e64 v103, v4, v43, s[4:5]
	v_cndmask_b32_e64 v102, v31, v42, s[4:5]
	v_cndmask_b32_e64 v105, v4, v45, s[6:7]
	v_cndmask_b32_e64 v104, v31, v44, s[6:7]
	v_cndmask_b32_e64 v107, v4, v47, s[8:9]
	v_cndmask_b32_e64 v106, v31, v46, s[8:9]
	v_cndmask_b32_e64 v109, v4, v49, s[10:11]
	v_cndmask_b32_e64 v108, v31, v48, s[10:11]
	s_mov_b64 s[4:5], 0
	v_add_u32_e32 v126, 0xc000, v2
	v_mov_b32_e32 v2, v3
	v_mov_b32_e32 v4, v3
	v_mov_b32_e32 v5, v3
	v_mov_b32_e32 v30, v3
	v_mov_b32_e32 v31, v3
	v_mov_b32_e32 v32, v3
	v_mov_b32_e32 v33, v3
	v_mov_b32_e32 v42, v3
	v_mov_b32_e32 v43, v3
	v_mov_b32_e32 v44, v3
	v_mov_b32_e32 v45, v3
	v_mov_b32_e32 v58, v3
	v_mov_b32_e32 v59, v3
	v_mov_b32_e32 v60, v3
	v_mov_b32_e32 v61, v3
	v_mov_b32_e32 v66, v3
	v_mov_b32_e32 v67, v3
	v_mov_b32_e32 v68, v3
	v_mov_b32_e32 v69, v3
	v_mov_b32_e32 v70, v3
	v_mov_b32_e32 v71, v3
	v_mov_b32_e32 v72, v3
	v_mov_b32_e32 v73, v3
	v_mov_b32_e32 v74, v3
	v_mov_b32_e32 v75, v3
	v_mov_b32_e32 v76, v3
	v_mov_b32_e32 v77, v3
	v_mov_b32_e32 v78, v3
	v_mov_b32_e32 v79, v3
	v_mov_b32_e32 v80, v3
	v_mov_b32_e32 v81, v3
	v_mov_b32_e32 v82, v3
	v_mov_b32_e32 v83, v3
	v_mov_b32_e32 v84, v3
	v_mov_b32_e32 v85, v3
	v_mov_b32_e32 v86, v3
	v_mov_b32_e32 v87, v3
	v_mov_b32_e32 v88, v3
	v_mov_b32_e32 v89, v3
	v_mov_b32_e32 v90, v3
	v_mov_b32_e32 v91, v3
	v_mov_b32_e32 v92, v3
	v_mov_b32_e32 v93, v3
	v_mov_b32_e32 v94, v3
	v_mov_b32_e32 v95, v3
	v_mov_b32_e32 v96, v3
	v_mov_b32_e32 v97, v3
	v_mov_b32_e32 v62, v3
	v_mov_b32_e32 v63, v3
	v_mov_b32_e32 v64, v3
	v_mov_b32_e32 v65, v3
	v_mov_b32_e32 v46, v3
	v_mov_b32_e32 v47, v3
	v_mov_b32_e32 v48, v3
	v_mov_b32_e32 v49, v3
	v_mov_b32_e32 v54, v3
	v_mov_b32_e32 v55, v3
	v_mov_b32_e32 v56, v3
	v_mov_b32_e32 v57, v3
	v_mov_b32_e32 v50, v3
	v_mov_b32_e32 v51, v3
	v_mov_b32_e32 v52, v3
	s_mov_b32 s60, 0
	s_mul_i32 s76, s31, 9
	s_add_i32 s63, s23, 2
	s_mul_i32 s73, s63, 11
	s_lshr_b32 s73, s73, 5
	s_mul_i32 s73, s73, 31
	s_add_i32 s62, s63, s73
	s_mov_b32 s64, 0
	s_mov_b32 s66, 1
	s_mov_b32 s67, 0
	s_add_i32 s75, s23, 6
	s_add_i32 s75, s75, s76
	s_lshl_b32 s68, s75, 14
	s_mov_b32 s69, 0
	v_lshl_add_u64 v[164:165], v[110:111], 0, s[68:69]
	s_add_i32 s70, s34, 0xc000
	v_lshl_add_u64 v[166:167], v[164:165], 0, s[2:3]
	v_mov_b32_e32 v160, v118

.Lc5_bar:
	s_barrier
	s_waitcnt lgkmcnt(5)
	v_mfma_f32_16x16x32_f16 v[94:97], v[10:13], v[18:21], v[94:97]
	ds_read_b128 v[128:131], v160
	v_mfma_f32_16x16x32_f16 v[90:93], v[6:9], v[18:21], v[90:93]
	v_xor_b32_e32 v162, 64, v119
	s_waitcnt lgkmcnt(5)
	v_mfma_f32_16x16x32_f16 v[78:81], v[10:13], v[14:17], v[78:81]
	ds_read_b128 v[132:135], v160 offset:2048
	v_mfma_f32_16x16x32_f16 v[74:77], v[6:9], v[14:17], v[74:77]
	v_xor_b32_e32 v163, 64, v120
	s_mov_b32 m0, s70
	s_add_i32 s71, s35, 0xffff8000
	global_load_lds_dwordx4 v[164:165], off
	s_waitcnt lgkmcnt(5)
	v_mfma_f32_16x16x32_f16 v[58:61], v[10:13], v[26:29], v[58:61]
	ds_read_b128 v[136:139], v162
	v_mfma_f32_16x16x32_f16 v[42:45], v[6:9], v[26:29], v[42:45]
	s_and_b32 s71, s71, 0xc000
	s_add_i32 s72, s70, 0x400
	s_waitcnt lgkmcnt(5)
	v_mfma_f32_16x16x32_f16 v[62:65], v[10:13], v[22:25], v[62:65]
	ds_read_b128 v[140:143], v162 offset:2048
	v_mfma_f32_16x16x32_f16 v[46:49], v[6:9], v[22:25], v[46:49]
	v_add_u32_e32 v161, s71, v117
	s_waitcnt lgkmcnt(5)
	v_mfma_f32_16x16x32_f16 v[86:89], v[38:41], v[18:21], v[86:89]
	ds_read_b128 v[144:147], v163
	s_waitcnt lgkmcnt(5)
	v_mfma_f32_16x16x32_f16 v[82:85], v[34:37], v[18:21], v[82:85]
	v_mfma_f32_16x16x32_f16 v[70:73], v[38:41], v[14:17], v[70:73]
	ds_read_b128 v[148:151], v163 offset:2048
	v_mfma_f32_16x16x32_f16 v[66:69], v[34:37], v[14:17], v[66:69]
	v_add_u32_e32 v168, s62, v115
	v_mfma_f32_16x16x32_f16 v[30:33], v[38:41], v[26:29], v[30:33]
	ds_read_b128 v[152:155], v160 offset:4096
	v_mfma_f32_16x16x32_f16 v[2:5], v[34:37], v[26:29], v[2:5]
	v_bitop3_b32 v169, v168, v114, 6 bitop3:0x6c
	v_lshl_add_u32 v168, v168, 7, s64
	v_mfma_f32_16x16x32_f16 v[54:57], v[38:41], v[22:25], v[54:57]
	ds_read_b128 v[156:159], v160 offset:6144
	v_mfma_f32_16x16x32_f16 v[50:53], v[34:37], v[22:25], v[50:53]
	v_lshl_or_b32 v119, v169, 4, v168
	v_add_u32_e32 v160, s71, v118
	s_waitcnt lgkmcnt(5)
	v_mfma_f32_16x16x32_f16 v[94:97], v[128:131], v[136:139], v[94:97]
	ds_read_b128 v[10:13], v161
	v_mfma_f32_16x16x32_f16 v[90:93], v[132:135], v[136:139], v[90:93]
	s_mov_b32 m0, s72
	s_add_i32 s63, s63, 2
	global_load_lds_dwordx4 v[166:167], off
	s_waitcnt lgkmcnt(5)
	v_mfma_f32_16x16x32_f16 v[78:81], v[128:131], v[140:143], v[78:81]
	ds_read_b128 v[6:9], v161 offset:2048
	v_mfma_f32_16x16x32_f16 v[74:77], v[132:135], v[140:143], v[74:77]
	v_add_u32_e32 v168, s62, v116
	s_waitcnt lgkmcnt(5)
	v_mfma_f32_16x16x32_f16 v[58:61], v[128:131], v[144:147], v[58:61]
	ds_read_b128 v[18:21], v119
	v_mfma_f32_16x16x32_f16 v[42:45], v[132:135], v[144:147], v[42:45]
	v_bitop3_b32 v169, v168, v114, 6 bitop3:0x6c
	v_lshl_add_u32 v168, v168, 7, s64
	s_waitcnt lgkmcnt(5)
	v_mfma_f32_16x16x32_f16 v[62:65], v[128:131], v[148:151], v[62:65]
	ds_read_b128 v[14:17], v119 offset:2048
	v_mfma_f32_16x16x32_f16 v[46:49], v[132:135], v[148:151], v[46:49]
	v_lshl_or_b32 v120, v169, 4, v168
	s_waitcnt lgkmcnt(5)
	v_mfma_f32_16x16x32_f16 v[86:89], v[152:155], v[136:139], v[86:89]
	ds_read_b128 v[26:29], v120
	s_waitcnt lgkmcnt(5)
	v_mfma_f32_16x16x32_f16 v[82:85], v[156:159], v[136:139], v[82:85]
	s_cmp_ge_u32 s63, 9
	s_cselect_b32 s73, 9, 0
	s_cselect_b32 s74, 0xc000, 0
	s_sub_i32 s63, s63, s73
	s_xor_b32 s64, s64, s74
	v_mfma_f32_16x16x32_f16 v[70:73], v[152:155], v[140:143], v[70:73]
	ds_read_b128 v[22:25], v120 offset:2048
	s_mul_i32 s73, s63, 11
	s_lshr_b32 s73, s73, 5
	s_mul_i32 s73, s73, 31
	s_add_i32 s62, s63, s73
	v_mfma_f32_16x16x32_f16 v[66:69], v[156:159], v[140:143], v[66:69]
	s_addk_i32 s35, 0x4000
	s_add_i32 s60, s60, 1
	s_add_i32 s75, s60, 3
	s_cmp_lt_u32 s60, 6
	s_cselect_b32 s75, s75, 8
	s_lshl_b32 s75, s75, 1
	s_add_i32 s75, s75, s23
	s_add_i32 s75, s75, s76
	s_lshl_b32 s68, s75, 14
	v_mfma_f32_16x16x32_f16 v[30:33], v[152:155], v[144:147], v[30:33]
	ds_read_b128 v[38:41], v161 offset:4096
	v_mfma_f32_16x16x32_f16 v[2:5], v[156:159], v[144:147], v[2:5]
	v_lshl_add_u64 v[164:165], v[110:111], 0, s[68:69]
	s_and_b32 s70, s35, 0xc000
	s_add_i32 s70, s70, s34
	v_mfma_f32_16x16x32_f16 v[54:57], v[152:155], v[148:151], v[54:57]
	ds_read_b128 v[34:37], v161 offset:6144
	v_lshl_add_u64 v[166:167], v[164:165], 0, s[2:3]
	v_mfma_f32_16x16x32_f16 v[50:53], v[156:159], v[148:151], v[50:53]
	s_cmp_lg_u32 s60, s66
	s_cbranch_scc1 .Lc5_nopatch
	v_readfirstlane_b32 s4, v121
	s_mov_b32 m0, s4
	v_readfirstlane_b32 s4, v122
	global_load_lds_dwordx4 v[98:99], off
	s_mov_b32 m0, s4
	v_readfirstlane_b32 s4, v123
	global_load_lds_dwordx4 v[100:101], off
	s_mov_b32 m0, s4
	v_readfirstlane_b32 s4, v124
	global_load_lds_dwordx4 v[102:103], off
	s_mov_b32 m0, s4
	v_readfirstlane_b32 s4, v125
	global_load_lds_dwordx4 v[104:105], off
	s_mov_b32 m0, s4
	v_readfirstlane_b32 s4, v126
	global_load_lds_dwordx4 v[106:107], off
	s_mov_b32 m0, s4
	s_mov_b64 s[4:5], -1
	global_load_lds_dwordx4 v[108:109], off
	s_movk_i32 s66, 0x3e8
	s_mov_b32 s67, 2

	.amdhsa_kernel _Z6conv_kILi256ELi128ELi3ELi64ELi1ELi2ELb0EEvPKDF16_S1_PKfS3_PDF16_S4_S1_fS3_S3_S3_S3_
		.amdhsa_group_segment_fixed_size 163840
		.amdhsa_private_segment_fixed_size 0
		.amdhsa_kernarg_size 96
		.amdhsa_user_sgpr_count 2
		.amdhsa_user_sgpr_dispatch_ptr 0
		.amdhsa_user_sgpr_queue_ptr 0
		.amdhsa_user_sgpr_kernarg_segment_ptr 1
		.amdhsa_user_sgpr_dispatch_id 0
		.amdhsa_user_sgpr_kernarg_preload_length 0
		.amdhsa_user_sgpr_kernarg_preload_offset 0
		.amdhsa_user_sgpr_private_segment_size 0
		.amdhsa_uses_dynamic_stack 0
		.amdhsa_enable_private_segment 0
		.amdhsa_system_sgpr_workgroup_id_x 1
		.amdhsa_system_sgpr_workgroup_id_y 0
		.amdhsa_system_sgpr_workgroup_id_z 0
		.amdhsa_system_sgpr_workgroup_info 0
		.amdhsa_system_vgpr_workitem_id 0
		.amdhsa_next_free_vgpr 172
		.amdhsa_next_free_sgpr 96
		.amdhsa_accum_offset 172
		.amdhsa_reserve_vcc 1
		.amdhsa_float_round_mode_32 0
		.amdhsa_float_round_mode_16_64 0
		.amdhsa_float_denorm_mode_32 3
		.amdhsa_float_denorm_mode_16_64 3
		.amdhsa_dx10_clamp 1
		.amdhsa_ieee_mode 1
		.amdhsa_fp16_overflow 0
		.amdhsa_tg_split 0
		.amdhsa_exception_fp_ieee_invalid_op 0
		.amdhsa_exception_fp_denorm_src 0
		.amdhsa_exception_fp_ieee_div_zero 0
		.amdhsa_exception_fp_ieee_overflow 0
		.amdhsa_exception_fp_ieee_underflow 0
		.amdhsa_exception_fp_ieee_inexact 0
		.amdhsa_exception_int_div_zero 0
	.end_amdhsa_kernel

amdhsa.kernels:
  - .agpr_count:     0
    .args:
      - .actual_access:  read_only
        .address_space:  global
        .offset:         0
        .size:           8
        .value_kind:     global_buffer
      - .actual_access:  read_only
        .address_space:  global
        .offset:         8
        .size:           8
        .value_kind:     global_buffer
      - .actual_access:  read_only
        .address_space:  global
        .offset:         16
        .size:           8
        .value_kind:     global_buffer
      - .actual_access:  read_only
        .address_space:  global
        .offset:         24
        .size:           8
        .value_kind:     global_buffer
      - .actual_access:  read_only
        .address_space:  global
        .offset:         32
        .size:           8
        .value_kind:     global_buffer
      - .actual_access:  read_only
        .address_space:  global
        .offset:         40
        .size:           8
        .value_kind:     global_buffer
      - .actual_access:  write_only
        .address_space:  global
        .offset:         48
        .size:           8
        .value_kind:     global_buffer
      - .actual_access:  write_only
        .address_space:  global
        .offset:         56
        .size:           8
        .value_kind:     global_buffer
      - .actual_access:  write_only
        .address_space:  global
        .offset:         64
        .size:           8
        .value_kind:     global_buffer
      - .actual_access:  write_only
        .address_space:  global
        .offset:         72
        .size:           8
        .value_kind:     global_buffer
      - .actual_access:  write_only
        .address_space:  global
        .offset:         80
        .size:           8
        .value_kind:     global_buffer
      - .actual_access:  write_only
        .address_space:  global
        .offset:         88
        .size:           8
        .value_kind:     global_buffer
      - .actual_access:  read_only
        .address_space:  global
        .offset:         96
        .size:           8
        .value_kind:     global_buffer
      - .actual_access:  read_only
        .address_space:  global
        .offset:         104
        .size:           8
        .value_kind:     global_buffer
      - .actual_access:  read_only
        .address_space:  global
        .offset:         112
        .size:           8
        .value_kind:     global_buffer
      - .actual_access:  read_only
        .address_space:  global
        .offset:         120
        .size:           8
        .value_kind:     global_buffer
      - .actual_access:  write_only
        .address_space:  global
        .offset:         128
        .size:           8
        .value_kind:     global_buffer
      - .actual_access:  write_only
        .address_space:  global
        .offset:         136
        .size:           8
        .value_kind:     global_buffer
    .group_segment_fixed_size: 14400
    .kernarg_segment_align: 8
    .kernarg_segment_size: 144
    .language:       OpenCL C
    .language_version:
      - 2
      - 0
    .max_flat_workgroup_size: 256
    .name:           _Z10prep_all_kPKfS0_S0_S0_S0_S0_PDF16_S1_S1_S1_S1_S1_S0_S0_S0_S0_S1_Pj
    .private_segment_fixed_size: 0
    .sgpr_count:     27
    .sgpr_spill_count: 0
    .symbol:         _Z10prep_all_kPKfS0_S0_S0_S0_S0_PDF16_S1_S1_S1_S1_S1_S0_S0_S0_S0_S1_Pj.kd
    .uniform_work_group_size: 1
    .uses_dynamic_stack: false
    .vgpr_count:     64
    .vgpr_spill_count: 0
    .wavefront_size: 64
  - .agpr_count:     0
    .args:
      - .actual_access:  read_only
        .address_space:  global
        .offset:         0
        .size:           8
        .value_kind:     global_buffer
      - .actual_access:  read_only
        .address_space:  global
        .offset:         8
        .size:           8
        .value_kind:     global_buffer
      - .actual_access:  read_only
        .address_space:  global
        .offset:         16
        .size:           8
        .value_kind:     global_buffer
      - .actual_access:  read_only
        .address_space:  global
        .offset:         24
        .size:           8
        .value_kind:     global_buffer
      - .actual_access:  read_only
        .address_space:  global
        .offset:         32
        .size:           8
        .value_kind:     global_buffer
      - .actual_access:  read_only
        .address_space:  global
        .offset:         40
        .size:           8
        .value_kind:     global_buffer
      - .actual_access:  write_only
        .address_space:  global
        .offset:         48
        .size:           8
        .value_kind:     global_buffer
    .group_segment_fixed_size: 0
    .kernarg_segment_align: 8
    .kernarg_segment_size: 56
    .language:       OpenCL C
    .language_version:
      - 2
      - 0
    .max_flat_workgroup_size: 256
    .name:           _Z9finish6_kPKDF16_PKfS2_S2_S2_S2_Pf
    .private_segment_fixed_size: 0
    .sgpr_count:     18
    .sgpr_spill_count: 0
    .symbol:         _Z9finish6_kPKDF16_PKfS2_S2_S2_S2_Pf.kd
    .uniform_work_group_size: 1
    .uses_dynamic_stack: false
    .vgpr_count:     51
    .vgpr_spill_count: 0
    .wavefront_size: 64
  - .agpr_count:     0
    .args:
      - .actual_access:  read_only
        .address_space:  global
        .offset:         0
        .size:           8
        .value_kind:     global_buffer
      - .actual_access:  write_only
        .address_space:  global
        .offset:         8
        .size:           8
        .value_kind:     global_buffer
    .group_segment_fixed_size: 16640
    .kernarg_segment_align: 8
    .kernarg_segment_size: 16
    .language:       OpenCL C
    .language_version:
      - 2
      - 0
    .max_flat_workgroup_size: 256
    .name:           _Z6gram_kPKfPf
    .private_segment_fixed_size: 0
    .sgpr_count:     16
    .sgpr_spill_count: 0
    .symbol:         _Z6gram_kPKfPf.kd
    .uniform_work_group_size: 1
    .uses_dynamic_stack: false
    .vgpr_count:     38
    .vgpr_spill_count: 0
    .wavefront_size: 64
  - .agpr_count:     0
    .args:
      - .actual_access:  read_only
        .address_space:  global
        .offset:         0
        .size:           8
        .value_kind:     global_buffer
      - .address_space:  global
        .offset:         8
        .size:           8
        .value_kind:     global_buffer
      - .actual_access:  read_only
        .address_space:  global
        .offset:         16
        .size:           8
        .value_kind:     global_buffer
      - .actual_access:  read_only
        .address_space:  global
        .offset:         24
        .size:           8
        .value_kind:     global_buffer
      - .actual_access:  read_only
        .address_space:  global
        .offset:         32
        .size:           8
        .value_kind:     global_buffer
      - .actual_access:  write_only
        .address_space:  global
        .offset:         40
        .size:           8
        .value_kind:     global_buffer
      - .actual_access:  read_only
        .address_space:  global
        .offset:         48
        .size:           8
        .value_kind:     global_buffer
      - .offset:         56
        .size:           4
        .value_kind:     by_value
      - .actual_access:  read_only
        .address_space:  global
        .offset:         64
        .size:           8
        .value_kind:     global_buffer
      - .actual_access:  read_only
        .address_space:  global
        .offset:         72
        .size:           8
        .value_kind:     global_buffer
      - .actual_access:  read_only
        .address_space:  global
        .offset:         80
        .size:           8
        .value_kind:     global_buffer
      - .actual_access:  read_only
        .address_space:  global
        .offset:         88
        .size:           8
        .value_kind:     global_buffer
    .group_segment_fixed_size: 147456
    .kernarg_segment_align: 8
    .kernarg_segment_size: 96
    .language:       OpenCL C
    .language_version:
      - 2
      - 0
    .max_flat_workgroup_size: 512
    .name:           _Z6conv_kILi64ELi128ELi20ELi128ELi4ELi4ELb1EEvPKDF16_S1_PKfS3_PDF16_S4_S1_fS3_S3_S3_S3_
    .private_segment_fixed_size: 0
    .sgpr_count:     43
    .sgpr_spill_count: 0
    .symbol:         _Z6conv_kILi64ELi128ELi20ELi128ELi4ELi4ELb1EEvPKDF16_S1_PKfS3_PDF16_S4_S1_fS3_S3_S3_S3_.kd
    .uniform_work_group_size: 1
    .uses_dynamic_stack: false
    .vgpr_count:     160
    .vgpr_spill_count: 0
    .wavefront_size: 64
  - .agpr_count:     0
    .args:
      - .actual_access:  read_only
        .address_space:  global
        .offset:         0
        .size:           8
        .value_kind:     global_buffer
      - .actual_access:  read_only
        .address_space:  global
        .offset:         8
        .size:           8
        .value_kind:     global_buffer
      - .actual_access:  read_only
        .address_space:  global
        .offset:         16
        .size:           8
        .value_kind:     global_buffer
      - .actual_access:  write_only
        .address_space:  global
        .offset:         24
        .size:           8
        .value_kind:     global_buffer
    .group_segment_fixed_size: 0
    .kernarg_segment_align: 8
    .kernarg_segment_size: 32
    .language:       OpenCL C
    .language_version:
      - 2
      - 0
    .max_flat_workgroup_size: 256
    .name:           _Z8finish_kILi128ELi4EEvPKDF16_PKfS3_PDF16_
    .private_segment_fixed_size: 0
    .sgpr_count:     18
    .sgpr_spill_count: 0
    .symbol:         _Z8finish_kILi128ELi4EEvPKDF16_PKfS3_PDF16_.kd
    .uniform_work_group_size: 1
    .uses_dynamic_stack: false
    .vgpr_count:     44
    .vgpr_spill_count: 0
    .wavefront_size: 64
  - .agpr_count:     0
    .args:
      - .address_space:  global
        .offset:         0
        .size:           8
        .value_kind:     global_buffer
      - .address_space:  global
        .offset:         8
        .size:           8
        .value_kind:     global_buffer
      - .address_space:  global
        .offset:         16
        .size:           8
        .value_kind:     global_buffer
      - .actual_access:  read_only
        .address_space:  global
        .offset:         24
        .size:           8
        .value_kind:     global_buffer
      - .actual_access:  write_only
        .address_space:  global
        .offset:         32
        .size:           8
        .value_kind:     global_buffer
      - .actual_access:  read_only
        .address_space:  global
        .offset:         40
        .size:           8
        .value_kind:     global_buffer
      - .address_space:  global
        .offset:         48
        .size:           8
        .value_kind:     global_buffer
      - .offset:         56
        .size:           4
        .value_kind:     by_value
      - .actual_access:  read_only
        .address_space:  global
        .offset:         64
        .size:           8
        .value_kind:     global_buffer
      - .actual_access:  read_only
        .address_space:  global
        .offset:         72
        .size:           8
        .value_kind:     global_buffer
      - .actual_access:  read_only
        .address_space:  global
        .offset:         80
        .size:           8
        .value_kind:     global_buffer
      - .actual_access:  read_only
        .address_space:  global
        .offset:         88
        .size:           8
        .value_kind:     global_buffer
    .group_segment_fixed_size: 163840
    .kernarg_segment_align: 8
    .kernarg_segment_size: 96
    .language:       OpenCL C
    .language_version:
      - 2
      - 0
    .max_flat_workgroup_size: 512
    .name:           _Z6conv_kILi128ELi256ELi3ELi64ELi1ELi1ELb0EEvPKDF16_S1_PKfS3_PDF16_S4_S1_fS3_S3_S3_S3_
    .private_segment_fixed_size: 0
    .sgpr_count:     51
    .sgpr_spill_count: 0
    .symbol:         _Z6conv_kILi128ELi256ELi3ELi64ELi1ELi1ELb0EEvPKDF16_S1_PKfS3_PDF16_S4_S1_fS3_S3_S3_S3_.kd
    .uniform_work_group_size: 1
    .uses_dynamic_stack: false
    .vgpr_count:     184
    .vgpr_spill_count: 0
    .wavefront_size: 64
  - .agpr_count:     0
    .args:
      - .address_space:  global
        .offset:         0
        .size:           8
        .value_kind:     global_buffer
      - .address_space:  global
        .offset:         8
        .size:           8
        .value_kind:     global_buffer
      - .address_space:  global
        .offset:         16
        .size:           8
        .value_kind:     global_buffer
      - .actual_access:  read_only
        .address_space:  global
        .offset:         24
        .size:           8
        .value_kind:     global_buffer
      - .actual_access:  write_only
        .address_space:  global
        .offset:         32
        .size:           8
        .value_kind:     global_buffer
      - .actual_access:  read_only
        .address_space:  global
        .offset:         40
        .size:           8
        .value_kind:     global_buffer
      - .address_space:  global
        .offset:         48
        .size:           8
        .value_kind:     global_buffer
      - .offset:         56
        .size:           4
        .value_kind:     by_value
      - .actual_access:  read_only
        .address_space:  global
        .offset:         64
        .size:           8
        .value_kind:     global_buffer
      - .actual_access:  read_only
        .address_space:  global
        .offset:         72
        .size:           8
        .value_kind:     global_buffer
      - .actual_access:  read_only
        .address_space:  global
        .offset:         80
        .size:           8
        .value_kind:     global_buffer
      - .actual_access:  read_only
        .address_space:  global
        .offset:         88
        .size:           8
        .value_kind:     global_buffer
    .group_segment_fixed_size: 163840
    .kernarg_segment_align: 8
    .kernarg_segment_size: 96
    .language:       OpenCL C
    .language_version:
      - 2
      - 0
    .max_flat_workgroup_size: 512
    .name:           _Z6conv_kILi256ELi512ELi3ELi128ELi1ELi1ELb0EEvPKDF16_S1_PKfS3_PDF16_S4_S1_fS3_S3_S3_S3_
    .private_segment_fixed_size: 0
    .sgpr_count:     64
    .sgpr_spill_count: 0
    .symbol:         _Z6conv_kILi256ELi512ELi3ELi128ELi1ELi1ELb0EEvPKDF16_S1_PKfS3_PDF16_S4_S1_fS3_S3_S3_S3_.kd
    .uniform_work_group_size: 1
    .uses_dynamic_stack: false
    .vgpr_count:     184
    .vgpr_spill_count: 0
    .wavefront_size: 64
  - .agpr_count:     0
    .args:
      - .address_space:  global
        .offset:         0
        .size:           8
        .value_kind:     global_buffer
      - .address_space:  global
        .offset:         8
        .size:           8
        .value_kind:     global_buffer
      - .address_space:  global
        .offset:         16
        .size:           8
        .value_kind:     global_buffer
      - .actual_access:  read_only
        .address_space:  global
        .offset:         24
        .size:           8
        .value_kind:     global_buffer
      - .actual_access:  write_only
        .address_space:  global
        .offset:         32
        .size:           8
        .value_kind:     global_buffer
      - .actual_access:  read_only
        .address_space:  global
        .offset:         40
        .size:           8
        .value_kind:     global_buffer
      - .address_space:  global
        .offset:         48
        .size:           8
        .value_kind:     global_buffer
      - .offset:         56
        .size:           4
        .value_kind:     by_value
      - .actual_access:  read_only
        .address_space:  global
        .offset:         64
        .size:           8
        .value_kind:     global_buffer
      - .actual_access:  read_only
        .address_space:  global
        .offset:         72
        .size:           8
        .value_kind:     global_buffer
      - .actual_access:  read_only
        .address_space:  global
        .offset:         80
        .size:           8
        .value_kind:     global_buffer
      - .actual_access:  read_only
        .address_space:  global
        .offset:         88
        .size:           8
        .value_kind:     global_buffer
    .group_segment_fixed_size: 163840
    .kernarg_segment_align: 8
    .kernarg_segment_size: 96
    .language:       OpenCL C
    .language_version:
      - 2
      - 0
    .max_flat_workgroup_size: 512
    .name:           _Z6conv_kILi512ELi256ELi3ELi64ELi1ELi1ELb0EEvPKDF16_S1_PKfS3_PDF16_S4_S1_fS3_S3_S3_S3_
    .private_segment_fixed_size: 0
    .sgpr_count:     66
    .sgpr_spill_count: 0
    .symbol:         _Z6conv_kILi512ELi256ELi3ELi64ELi1ELi1ELb0EEvPKDF16_S1_PKfS3_PDF16_S4_S1_fS3_S3_S3_S3_.kd
    .uniform_work_group_size: 1
    .uses_dynamic_stack: false
    .vgpr_count:     184
    .vgpr_spill_count: 0
    .wavefront_size: 64
  - .agpr_count:     0
    .args:
      - .address_space:  global
        .offset:         0
        .size:           8
        .value_kind:     global_buffer
      - .address_space:  global
        .offset:         8
        .size:           8
        .value_kind:     global_buffer
      - .actual_access:  read_only
        .address_space:  global
        .offset:         16
        .size:           8
        .value_kind:     global_buffer
      - .actual_access:  read_only
        .address_space:  global
        .offset:         24
        .size:           8
        .value_kind:     global_buffer
      - .actual_access:  read_only
        .address_space:  global
        .offset:         32
        .size:           8
        .value_kind:     global_buffer
      - .actual_access:  write_only
        .address_space:  global
        .offset:         40
        .size:           8
        .value_kind:     global_buffer
      - .address_space:  global
        .offset:         48
        .size:           8
        .value_kind:     global_buffer
      - .offset:         56
        .size:           4
        .value_kind:     by_value
      - .actual_access:  read_only
        .address_space:  global
        .offset:         64
        .size:           8
        .value_kind:     global_buffer
      - .actual_access:  read_only
        .address_space:  global
        .offset:         72
        .size:           8
        .value_kind:     global_buffer
      - .actual_access:  read_only
        .address_space:  global
        .offset:         80
        .size:           8
        .value_kind:     global_buffer
      - .actual_access:  read_only
        .address_space:  global
        .offset:         88
        .size:           8
        .value_kind:     global_buffer
    .group_segment_fixed_size: 163840
    .kernarg_segment_align: 8
    .kernarg_segment_size: 96
    .language:       OpenCL C
    .language_version:
      - 2
      - 0
    .max_flat_workgroup_size: 512
    .name:           _Z6conv_kILi256ELi128ELi3ELi64ELi1ELi2ELb0EEvPKDF16_S1_PKfS3_PDF16_S4_S1_fS3_S3_S3_S3_
    .private_segment_fixed_size: 0
    .sgpr_count:     55
    .sgpr_spill_count: 0
    .symbol:         _Z6conv_kILi256ELi128ELi3ELi64ELi1ELi2ELb0EEvPKDF16_S1_PKfS3_PDF16_S4_S1_fS3_S3_S3_S3_.kd
    .uniform_work_group_size: 1
    .uses_dynamic_stack: false
    .vgpr_count:     172
    .vgpr_spill_count: 0
    .wavefront_size: 64
  - .agpr_count:     0
    .args:
      - .actual_access:  read_only
        .address_space:  global
        .offset:         0
        .size:           8
        .value_kind:     global_buffer
      - .actual_access:  read_only
        .address_space:  global
        .offset:         8
        .size:           8
        .value_kind:     global_buffer
      - .actual_access:  read_only
        .address_space:  global
        .offset:         16
        .size:           8
        .value_kind:     global_buffer
      - .actual_access:  write_only
        .address_space:  global
        .offset:         24
        .size:           8
        .value_kind:     global_buffer
    .group_segment_fixed_size: 0
    .kernarg_segment_align: 8
    .kernarg_segment_size: 32
    .language:       OpenCL C
    .language_version:
      - 2
      - 0
    .max_flat_workgroup_size: 256
    .name:           _Z8finish_kILi128ELi2EEvPKDF16_PKfS3_PDF16_
    .private_segment_fixed_size: 0
    .sgpr_count:     18
    .sgpr_spill_count: 0
    .symbol:         _Z8finish_kILi128ELi2EEvPKDF16_PKfS3_PDF16_.kd
    .uniform_work_group_size: 1
    .uses_dynamic_stack: false
    .vgpr_count:     28
    .vgpr_spill_count: 0
    .wavefront_size: 64
  - .agpr_count:     0
    .args:
      - .address_space:  global
        .offset:         0
        .size:           8
        .value_kind:     global_buffer
      - .address_space:  global
        .offset:         8
        .size:           8
        .value_kind:     global_buffer
      - .actual_access:  read_only
        .address_space:  global
        .offset:         16
        .size:           8
        .value_kind:     global_buffer
      - .actual_access:  read_only
        .address_space:  global
        .offset:         24
        .size:           8
        .value_kind:     global_buffer
      - .actual_access:  read_only
        .address_space:  global
        .offset:         32
        .size:           8
        .value_kind:     global_buffer
      - .actual_access:  write_only
        .address_space:  global
        .offset:         40
        .size:           8
        .value_kind:     global_buffer
      - .address_space:  global
        .offset:         48
        .size:           8
        .value_kind:     global_buffer
      - .offset:         56
        .size:           4
        .value_kind:     by_value
      - .actual_access:  read_only
        .address_space:  global
        .offset:         64
        .size:           8
        .value_kind:     global_buffer
      - .actual_access:  read_only
        .address_space:  global
        .offset:         72
        .size:           8
        .value_kind:     global_buffer
      - .actual_access:  read_only
        .address_space:  global
        .offset:         80
        .size:           8
        .value_kind:     global_buffer
      - .actual_access:  read_only
        .address_space:  global
        .offset:         88
        .size:           8
        .value_kind:     global_buffer
    .group_segment_fixed_size: 147456
    .kernarg_segment_align: 8
    .kernarg_segment_size: 96
    .language:       OpenCL C
    .language_version:
      - 2
      - 0
    .max_flat_workgroup_size: 512
    .name:           _Z6conv_kILi128ELi64ELi20ELi64ELi4ELi4ELb0EEvPKDF16_S1_PKfS3_PDF16_S4_S1_fS3_S3_S3_S3_
    .private_segment_fixed_size: 0
    .sgpr_count:     64
    .sgpr_spill_count: 0
    .symbol:         _Z6conv_kILi128ELi64ELi20ELi64ELi4ELi4ELb0EEvPKDF16_S1_PKfS3_PDF16_S4_S1_fS3_S3_S3_S3_.kd
    .uniform_work_group_size: 1
    .uses_dynamic_stack: false
    .vgpr_count:     184
    .vgpr_spill_count: 0
    .wavefront_size: 64
